# per-query tie loop: tie-mask LDS read issued together with the threshold-entry read; on top of v24
# baseline (speedup 1.0000x reference)
.LBB0_584:
	v_readlane_b32 s0, v251, 50
	s_add_i32 s12, s41, s0
	s_lshl_b32 s0, s12, 4
	s_add_i32 s0, s0, 0
	s_add_i32 s0, s0, 0x23000
	v_mov_b32_e32 v0, s0
	ds_read_b96 v[12:14], v0
	s_lshl_b32 s0, s12, 7
	v_lshl_add_u32 v0, s0, 2, v10
	ds_read_b64 v[4:5], v0 offset:32768
	s_lshl_b32 s0, s12, 9
	s_add_i32 s50, s0, 0
	s_add_i32 s46, s50, 0x18000
	s_waitcnt lgkmcnt(1)
	v_readfirstlane_b32 s47, v13
	v_readfirstlane_b32 s13, v12
	s_cmp_lt_i32 s47, 1
	v_readfirstlane_b32 s51, v14
	s_cbranch_scc1 .LBB0_700
	s_lshl_b32 s0, s12, 7
	v_lshl_add_u32 v0, s0, 2, v10
	s_cmp_lt_i32 s47, s51
	s_mov_b64 s[0:1], -1
	s_cbranch_scc1 .LBB0_587
	v_lshl_add_u32 v0, v6, 2, s46
	ds_read_b64 v[12:13], v0
	s_mov_b64 s[0:1], 0
	s_waitcnt lgkmcnt(0)
	v_or_b32_e32 v13, v13, v5
	v_or_b32_e32 v12, v12, v4
	ds_write_b64 v0, v[12:13]
